# phase H top-k unit: the four query-tile loads of a thread issued together instead of a load-wait-write loop
# speedup vs baseline: 1.0030x; 1.0030x over previous
.LBB0_974:
	s_or_b64 exec, exec, s[18:19]
	s_movk_i32 s18, 0x800
	s_ashr_i32 s76, s52, 3
	s_and_b32 s28, s52, 7
	v_cmp_gt_i32_e32 vcc, s18, v2
	s_and_saveexec_b64 s[18:19], vcc
	s_movk_i32 s78, 0x210
	s_cbranch_execz .LBB0_977
	s_lshl_b32 s77, s76, 6
	s_lshl_b32 s50, s28, 9
	s_add_u32 s50, s26, s50
	v_readlane_b32 s27, v255, 22
	s_addc_u32 s51, s27, 0
	v_lshlrev_b32_e32 v0, 3, v2
	s_mov_b64 s[70:71], 0
	v_mov_b32_e32 v1, v2
	v_ashrrev_i32_e32 v3, 5, v1
	v_lshlrev_b32_e32 v5, 1, v0
	v_add_u32_e32 v4, s77, v3
	v_and_b32_e32 v104, 0x1f0, v5
	v_ashrrev_i32_e32 v5, 31, v4
	v_lshlrev_b64 v[4:5], 12, v[4:5]
	v_lshl_add_u64 v[4:5], s[50:51], 0, v[4:5]
	v_lshl_add_u64 v[126:127], v[4:5], 0, v[104:105]
	s_mov_b64 s[70:71], 0x10000
	global_load_dwordx4 v[110:113], v[126:127], off
	v_lshl_add_u64 v[128:129], v[126:127], 0, s[70:71]
	global_load_dwordx4 v[114:117], v[128:129], off
	v_lshl_add_u64 v[130:131], v[128:129], 0, s[70:71]
	global_load_dwordx4 v[118:121], v[130:131], off
	v_lshl_add_u64 v[132:133], v[130:131], 0, s[70:71]
	global_load_dwordx4 v[122:125], v[132:133], off
	v_mul_lo_u32 v3, v3, s78
	v_add3_u32 v3, v12, v3, v104
	s_waitcnt vmcnt(3)
	ds_write_b128 v3, v[110:113]
	s_waitcnt vmcnt(2)
	ds_write_b128 v3, v[114:117] offset:8448
	s_waitcnt vmcnt(1)
	ds_write_b128 v3, v[118:121] offset:16896
	s_waitcnt vmcnt(0)
	ds_write_b128 v3, v[122:125] offset:25344

.LBB0_1033:
	s_or_b64 exec, exec, s[18:19]
	s_movk_i32 s18, 0x800
	s_ashr_i32 s28, s52, 3
	s_and_b32 s26, s52, 7
	v_cmp_gt_i32_e32 vcc, s18, v2
	s_and_saveexec_b64 s[18:19], vcc
	s_movk_i32 s76, 0x210
	s_cbranch_execz .LBB0_1036
	s_lshl_b32 s36, s28, 6
	s_lshl_b32 s40, s26, 9
	s_add_u32 s50, s27, s40
	v_readlane_b32 s40, v255, 33
	s_addc_u32 s51, s40, 0
	v_lshlrev_b32_e32 v0, 3, v2
	s_mov_b64 s[70:71], 0
	v_mov_b32_e32 v1, v2
	v_ashrrev_i32_e32 v3, 5, v1
	v_lshlrev_b32_e32 v5, 1, v0
	v_add_u32_e32 v4, s36, v3
	v_and_b32_e32 v104, 0x1f0, v5
	v_ashrrev_i32_e32 v5, 31, v4
	v_lshlrev_b64 v[4:5], 12, v[4:5]
	v_lshl_add_u64 v[4:5], s[50:51], 0, v[4:5]
	v_lshl_add_u64 v[126:127], v[4:5], 0, v[104:105]
	s_mov_b64 s[70:71], 0x10000
	global_load_dwordx4 v[110:113], v[126:127], off
	v_lshl_add_u64 v[128:129], v[126:127], 0, s[70:71]
	global_load_dwordx4 v[114:117], v[128:129], off
	v_lshl_add_u64 v[130:131], v[128:129], 0, s[70:71]
	global_load_dwordx4 v[118:121], v[130:131], off
	v_lshl_add_u64 v[132:133], v[130:131], 0, s[70:71]
	global_load_dwordx4 v[122:125], v[132:133], off
	v_mul_lo_u32 v3, v3, s76
	v_add3_u32 v3, v12, v3, v104
	s_waitcnt vmcnt(3)
	ds_write_b128 v3, v[110:113]
	s_waitcnt vmcnt(2)
	ds_write_b128 v3, v[114:117] offset:8448
	s_waitcnt vmcnt(1)
	ds_write_b128 v3, v[118:121] offset:16896
	s_waitcnt vmcnt(0)
	ds_write_b128 v3, v[122:125] offset:25344
